# attention unit remap for L2 locality + single-lane padding LDS-DMA loads
# speedup vs baseline: 1.0080x; 1.0080x over previous
.LBB0_16:
	s_or_b64 exec, exec, s[0:1]
	s_cmp_lt_i32 s88, 32
	s_cselect_b64 s[0:1], -1, 0
	s_ashr_i32 s79, s78, 31
	v_writelane_b32 v252, s0, 0
	s_ashr_i32 s89, s88, 31
	s_add_i32 s6, s88, s78
	v_writelane_b32 v252, s1, 1
	s_lshl_b64 s[0:1], s[78:79], 9
	v_writelane_b32 v252, s0, 2
	s_lshl_b32 s83, s88, 3
	s_lshl_b32 s94, s78, 3
	v_writelane_b32 v252, s1, 3
	s_lshl_b64 s[0:1], s[88:89], 9
	v_writelane_b32 v252, s0, 4
	s_cmp_gt_i32 s73, 1
	s_mov_b32 s93, 0
	v_writelane_b32 v252, s1, 5
	s_cselect_b64 s[0:1], -1, 0
	v_writelane_b32 v252, s0, 6
	s_cmpk_lt_i32 s82, 0xa00
	v_mbcnt_lo_u32_b32 v1, -1, 0
	v_writelane_b32 v252, s1, 7
	s_cselect_b64 s[0:1], -1, 0
	v_writelane_b32 v252, s0, 8
	s_ashr_i32 s15, s82, 31
	v_mov_b32_e32 v3, 0
	v_writelane_b32 v252, s1, 9
	s_lshr_b32 s0, s15, 29
	s_add_i32 s0, s82, s0
	s_ashr_i32 s2, s0, 3
	s_and_b32 s0, s0, -8
	s_sub_i32 s3, s82, s0
	s_cmpk_lt_i32 s82, 0x300
	s_cselect_b64 s[0:1], -1, 0
	v_writelane_b32 v252, s0, 10
	s_cmpk_lt_i32 s82, 0x400
	v_mov_b32_e32 v246, 0x7f800000
	v_writelane_b32 v252, s1, 11
	s_cselect_b64 s[0:1], -1, 0
	v_writelane_b32 v252, s0, 12
	v_mov_b32_e32 v239, 0x3c0881c4
	v_mov_b32_e32 v236, 0xbab64f3b
	v_writelane_b32 v252, s1, 13
	s_lshl_b32 s0, s3, 7
	s_cmpk_lt_i32 s82, 0x200
	s_cselect_b64 s[4:5], -1, 0
	v_writelane_b32 v252, s4, 14
	s_lshl_b32 s1, s3, 6
	v_mov_b32_e32 v234, 0x358637bd
	v_writelane_b32 v252, s5, 15
	s_not_b32 s4, s82
	s_cmpk_lt_i32 s82, 0x800
	s_cselect_b64 s[8:9], -1, 0
	s_lshl_b32 s5, s82, 5
	v_writelane_b32 v252, s8, 16
	s_and_b32 s5, s5, 0xf00
	s_sub_i32 s7, 0xf00, s5
	v_writelane_b32 v252, s9, 17
	s_sub_i32 s5, 0x1000, s5
	s_and_b32 s10, s82, 7
	v_writelane_b32 v252, s7, 18
	s_ashr_i32 s5, s5, 6
	v_writelane_b32 v252, s5, 19
	s_lshl_b32 s5, s10, 8
	v_writelane_b32 v252, s5, 20
	s_lshl_b32 s5, s78, 1
	s_bfe_u32 s9, s82, 0x40007
	s_add_i32 s5, s5, s4
	s_cmpk_lt_i32 s5, 0x800
	s_cselect_b64 s[12:13], -1, 0
	s_lshl_b32 s8, s5, 5
	s_and_b32 s8, s8, 0xf00
	v_writelane_b32 v252, s12, 21
	s_sub_i32 s8, 0x1000, s8
	s_ashr_i32 s8, s8, 6
	v_writelane_b32 v252, s13, 22
	v_writelane_b32 v252, s8, 23
	s_lshl_b32 s8, s5, 8
	s_and_b32 s8, s8, 0x700
	v_writelane_b32 v252, s8, 24
	s_add_i32 s4, s78, s4
	v_writelane_b32 v252, s4, 25
	v_writelane_b32 v252, s9, 26
	s_lshl_b32 s4, s9, 24
	v_writelane_b32 v252, s4, 27
	v_writelane_b32 v252, s10, 28
	s_lshl_b32 s4, s10, 7
	v_writelane_b32 v252, s4, 29
	s_lshl_b32 s4, s5, 17
	s_and_b32 s4, s4, 0xf000000
	v_writelane_b32 v252, s4, 30
	s_lshl_b32 s4, s5, 7
	s_bfe_u32 s7, s5, 0x40007
	s_and_b32 s4, s4, 0x380
	s_cmpk_lt_i32 s82, 0xc00
	v_writelane_b32 v252, s4, 31
	s_cselect_b64 s[4:5], -1, 0
	v_writelane_b32 v252, s4, 32
	s_cmpk_lt_i32 s88, 0x100
	v_mov_b32_e32 v237, 0x3727c5ac
	v_writelane_b32 v252, s5, 33
	s_cselect_b64 s[4:5], -1, 0
	v_writelane_b32 v252, s4, 34
	s_ashr_i32 s10, s88, 2
	s_mov_b32 s8, s10
	v_writelane_b32 v252, s5, 35
	s_and_b32 s4, s88, 3
	s_lshl_b32 s5, s4, 18
	v_writelane_b32 v252, s5, 36
	s_lshl_b32 s5, s10, 8
	v_writelane_b32 v252, s5, 37
	s_lshl_b32 s5, s4, 7
	v_writelane_b32 v252, s5, 38
	s_ashr_i32 s11, s10, 31
	v_writelane_b32 v252, s8, 39
	s_lshl_b32 s4, s4, 8
	s_lshl_b32 s26, s78, 9
	v_writelane_b32 v252, s9, 40
	s_lshl_b64 s[8:9], s[10:11], 18
	v_writelane_b32 v252, s8, 41
	s_cmp_lt_i32 s3, 0
	s_mul_i32 s5, s3, 0x41
	v_writelane_b32 v252, s9, 42
	s_movk_i32 s8, 0x141
	v_writelane_b32 v252, s4, 43
	s_mul_i32 s4, s3, 0x81
	s_cselect_b32 s8, s8, 0x140
	s_mul_i32 s8, s3, s8
	s_movk_i32 s9, 0x61
	s_cselect_b32 s10, s4, s0
	s_movk_i32 s0, 0x181
	s_cselect_b32 s9, s9, 0x60
	s_cselect_b32 s11, s5, s1
	s_cselect_b32 s12, s0, 0x180
	s_add_i32 s8, s8, s2
	s_mul_hi_i32 s0, s8, 0x66666667
	s_lshr_b32 s1, s0, 31
	s_ashr_i32 s0, s0, 5
	s_add_i32 s0, s0, s1
	s_mul_i32 s1, s0, 0x50
	s_sub_i32 s1, s8, s1
	s_bfe_i32 s4, s1, 0x80000
	s_bfe_u32 s4, s4, 0x3000c
	s_add_i32 s5, s1, s4
	s_bfe_i32 s4, s5, 0x80000
	s_sext_i32_i16 s8, s4
	s_lshr_b32 s4, s8, 3
	s_and_b32 s5, s5, 0xf8
	s_sub_i32 s1, s1, s5
	s_bfe_i64 s[4:5], s[4:5], 0x100000
	s_lshl_b32 s0, s0, 3
	s_sext_i32_i8 s1, s1
	s_lshl_b64 s[4:5], s[4:5], 18
	s_add_i32 s0, s0, s1
	v_writelane_b32 v252, s4, 44
	s_ashr_i32 s8, s8, 3
	s_ashr_i32 s1, s0, 31
	v_writelane_b32 v252, s5, 45
	s_lshl_b32 s4, s0, 8
	v_writelane_b32 v252, s4, 46
	v_writelane_b32 v252, s8, 47
	s_lshl_b32 s4, s8, 8
	v_writelane_b32 v252, s4, 48
	s_lshl_b64 s[4:5], s[0:1], 18
	v_writelane_b32 v252, s4, 49
	s_cmp_lt_i32 s0, 64
	s_mul_i32 s1, s3, s9
	v_writelane_b32 v252, s5, 50
	s_cselect_b64 s[4:5], -1, 0
	v_writelane_b32 v252, s4, 51
	s_add_i32 s1, s1, s2
	s_mul_i32 s3, s3, s12
	v_writelane_b32 v252, s5, 52
	s_mul_hi_i32 s4, s1, 0x2aaaaaab
	s_lshr_b32 s5, s4, 31
	s_ashr_i32 s4, s4, 2
	s_add_i32 s4, s4, s5
	s_mul_i32 s5, s4, 24
	s_sub_i32 s1, s1, s5
	s_bfe_i32 s5, s1, 0x80000
	s_bfe_u32 s5, s5, 0x3000c
	s_add_i32 s5, s1, s5
	s_and_b32 s8, s5, 0xf8
	s_sub_i32 s1, s1, s8
	s_add_i32 s8, s10, s2
	s_ashr_i32 s9, s8, 31
	s_lshr_b32 s9, s9, 27
	s_add_i32 s9, s8, s9
	s_and_b32 s10, s9, 0xffe0
	s_sub_i32 s8, s8, s10
	s_bfe_i32 s10, s8, 0x80000
	s_bfe_u32 s10, s10, 0x3000c
	s_add_i32 s10, s8, s10
	s_and_b32 s13, s10, 0xf8
	s_add_i32 s3, s3, s2
	s_sub_i32 s13, s8, s13
	s_add_i32 s8, s11, s2
	s_mul_hi_i32 s2, s3, 0x2aaaaaab
	s_lshr_b32 s11, s2, 31
	s_ashr_i32 s2, s2, 4
	s_add_i32 s11, s2, s11
	s_mul_i32 s2, s11, 0x60
	s_sub_i32 s2, s3, s2
	s_bfe_i32 s3, s2, 0x80000
	s_bfe_u32 s3, s3, 0x3000c
	s_add_i32 s12, s2, s3
	s_sub_i32 s92, s0, 64
	s_lshl_b32 s0, s4, 3
	s_sext_i32_i8 s1, s1
	s_and_b32 s3, s12, 0xf8
	s_add_i32 s0, s0, s1
	s_sub_i32 s14, s2, s3
	s_ashr_i32 s1, s0, 31
	s_lshl_b32 s3, s0, 8
	s_bfe_i32 s2, s5, 0x80000
	v_writelane_b32 v252, s3, 53
	s_lshl_b64 s[0:1], s[0:1], 20
	s_sext_i32_i16 s2, s2
	v_writelane_b32 v252, s0, 54
	s_ashr_i32 s16, s2, 3
	s_ashr_i32 s4, s8, 31
	v_writelane_b32 v252, s1, 55
	s_lshr_b32 s0, s2, 3
	s_bfe_i64 s[0:1], s[0:1], 0x100000
	s_lshl_b64 s[0:1], s[0:1], 17
	v_writelane_b32 v252, s0, 56
	s_lshr_b32 s4, s4, 28
	s_add_i32 s4, s8, s4
	v_writelane_b32 v252, s1, 57
	s_bfe_i32 s1, s10, 0x80000
	s_lshl_b32 s10, s11, 3
	s_bfe_i32 s11, s12, 0x80000
	s_sext_i32_i16 s12, s11
	s_lshr_b32 s12, s12, 3
	s_sext_i32_i16 s2, s1
	s_sext_i32_i8 s1, s13
	s_lshl_b32 s13, s12, 8
	v_writelane_b32 v252, s13, 58
	s_bfe_i64 s[12:13], s[12:13], 0x100000
	s_lshl_b64 s[12:13], s[12:13], 18
	s_ashr_i32 s0, s9, 5
	v_writelane_b32 v252, s12, 59
	s_lshl_b32 s0, s0, 3
	s_add_i32 s0, s0, s1
	v_writelane_b32 v252, s13, 60
	v_writelane_b32 v252, s16, 61
	s_lshl_b32 s12, s16, 8
	s_ashr_i32 s9, s2, 3
	v_writelane_b32 v252, s12, 62
	s_lshl_b32 s12, s0, 8
	s_sext_i32_i8 s11, s14
	v_writelane_b32 v252, s12, 63
	s_lshl_b32 s12, s9, 8
	s_add_i32 s10, s10, s11
	v_writelane_b32 v253, s12, 0
	s_lshl_b32 s12, s8, 8
	v_writelane_b32 v253, s12, 1
	s_lshl_b32 s12, s10, 8
	v_writelane_b32 v253, s12, 2
	s_lshl_b64 s[12:13], s[92:93], 18
	s_ashr_i32 s1, s0, 31
	v_writelane_b32 v253, s12, 3
	s_lshr_b32 s2, s2, 3
	s_bfe_i64 s[2:3], s[2:3], 0x100000
	v_writelane_b32 v253, s13, 4
	s_lshl_b64 s[12:13], s[0:1], 20
	v_writelane_b32 v253, s12, 5
	s_ashr_i32 s4, s4, 4
	s_ashr_i32 s5, s4, 31
	v_writelane_b32 v253, s13, 6
	s_lshl_b64 s[12:13], s[2:3], 16
	v_writelane_b32 v253, s12, 7
	s_ashr_i32 s11, s10, 31
	v_not_b32_e32 v233, 63
	v_writelane_b32 v253, s13, 8
	s_lshl_b64 s[12:13], s[4:5], 17
	v_writelane_b32 v253, s12, 9
	s_mul_hi_i32 s5, s4, 0x30000
	s_mul_i32 s4, s4, 0x30000
	v_writelane_b32 v253, s13, 10
	s_lshl_b64 s[12:13], s[10:11], 18
	v_writelane_b32 v253, s12, 11
	s_cmp_lt_i32 s10, 64
	v_not_b32_e32 v240, 31
	v_writelane_b32 v253, s13, 12
	s_cselect_b64 s[12:13], -1, 0
	s_sub_i32 s92, s10, 64
	s_abs_i32 s10, s78
	v_cvt_f32_u32_e32 v0, s10
	v_writelane_b32 v253, s12, 13
	v_mov_b32_e32 v241, 0x7fc00000
	v_mbcnt_hi_u32_b32 v242, -1, v1
	v_rcp_iflag_f32_e32 v0, v0
	v_writelane_b32 v253, s13, 14
	v_writelane_b32 v253, s5, 15
	v_writelane_b32 v253, s4, 16
	v_mul_f32_e32 v0, 0x4f7ffffe, v0
	v_cvt_u32_f32_e32 v0, v0
	s_sub_i32 s4, 0, s10
	v_mov_b32_e32 v243, 0xf149f2ca
	v_mov_b32_e32 v244, 0x1120000
	v_readfirstlane_b32 s5, v0
	s_mul_i32 s4, s4, s5
	s_mul_hi_u32 s4, s5, s4
	s_add_i32 s11, s5, s4
	s_lshl_b32 s4, s9, 1
	s_ashr_i32 s5, s4, 31
	s_lshl_b64 s[4:5], s[4:5], 19
	v_writelane_b32 v253, s4, 17
	v_mov_b32_e32 v245, 0x1110000
	v_mov_b32_e32 v247, 0x43e00000
	v_writelane_b32 v253, s5, 18
	s_mul_hi_i32 s4, s0, 0xc0000
	v_writelane_b32 v253, s4, 19
	s_mul_i32 s4, s0, 0xc0000
	v_writelane_b32 v253, s4, 20
	s_lshl_b64 s[0:1], s[0:1], 19
	v_writelane_b32 v253, s0, 21
	s_movk_i32 s84, 0xc00
	s_mov_b32 s85, 0x800000
	v_writelane_b32 v253, s1, 22
	s_lshl_b64 s[0:1], s[2:3], 19
	v_writelane_b32 v253, s0, 23
	s_lshl_b64 s[2:3], s[92:93], 18
	s_movk_i32 s86, 0x7fff
	v_writelane_b32 v253, s1, 24
	s_lshr_b32 s0, s11, 27
	s_mul_i32 s0, s0, s10
	s_sub_i32 s0, 32, s0
	s_sub_i32 s1, s0, s10
	s_cmp_ge_u32 s0, s10
	s_cselect_b32 s0, s1, s0
	s_sub_i32 s1, s0, s10
	s_cmp_ge_u32 s0, s10
	s_cselect_b32 s0, s1, s0
	s_sub_i32 s0, s6, s0
	v_writelane_b32 v253, s2, 25
	s_abs_i32 s1, s0
	s_ashr_i32 s0, s0, 31
	v_writelane_b32 v253, s3, 26
	s_mul_hi_u32 s2, s1, s11
	s_mul_i32 s2, s2, s10
	s_sub_i32 s1, s1, s2
	s_sub_i32 s2, s1, s10
	s_cmp_ge_u32 s1, s10
	s_cselect_b32 s1, s2, s1
	s_sub_i32 s2, s1, s10
	s_cmp_ge_u32 s1, s10
	s_cselect_b32 s1, s2, s1
	s_xor_b32 s1, s1, s0
	v_writelane_b32 v253, s11, 27
	s_sub_i32 s0, s1, s0
	v_writelane_b32 v253, s10, 28
	s_cmpk_lt_i32 s0, 0x58
	v_writelane_b32 v253, s0, 29
	s_cselect_b64 s[0:1], -1, 0
	v_writelane_b32 v253, s0, 30
	s_ashr_i32 s95, s94, 31
	s_mov_b32 s87, 0xffff0000
	v_writelane_b32 v253, s1, 31
	s_lshl_b32 s0, s88, 10
	v_writelane_b32 v253, s0, 32
	s_lshl_b32 s0, s78, 10
	v_writelane_b32 v253, s0, 33
	s_lshl_b64 s[0:1], s[94:95], 10
	v_writelane_b32 v253, s0, 34
	s_mov_b32 s55, 0xda24260
	s_mov_b32 s80, 0x42fe0000
	v_writelane_b32 v253, s1, 35
	s_lshl_b64 s[0:1], s[94:95], 12
	v_writelane_b32 v253, s0, 36
	s_mov_b32 s76, s93
	s_nop 0
	v_writelane_b32 v253, s1, 37
	s_lshl_b64 s[0:1], s[88:89], 10
	s_add_u32 s0, s0, 0x1120000
	v_writelane_b32 v253, s0, 38
	s_addc_u32 s0, s1, 0
	v_writelane_b32 v253, s0, 39
	s_lshl_b32 s0, s88, 9
	v_writelane_b32 v253, s0, 40
	s_lshl_b32 s0, s88, 4
	v_writelane_b32 v253, s0, 41
	s_lshl_b32 s0, s78, 4
	v_writelane_b32 v253, s0, 42
	s_lshl_b64 s[0:1], s[88:89], 14
	v_writelane_b32 v253, s0, 43
	s_lshl_b64 s[56:57], s[78:79], 10
	s_nop 0
	v_writelane_b32 v253, s1, 44
	s_lshl_b64 s[0:1], s[78:79], 14
	v_writelane_b32 v253, s0, 45
	s_nop 1
	v_writelane_b32 v253, s1, 46
	s_lshl_b64 s[0:1], s[88:89], 11
	s_add_u32 s0, s0, 0x3da00000
	v_writelane_b32 v253, s0, 47
	s_addc_u32 s0, s1, 0
	v_writelane_b32 v253, s0, 48
	s_mul_i32 s0, s7, 0x840000
	v_writelane_b32 v253, s0, 49
	s_mul_hi_i32 s0, s8, 0x30000
	v_writelane_b32 v253, s0, 50
	s_mul_i32 s0, s8, 0x30000
	v_writelane_b32 v253, s0, 51
	s_lshl_b64 s[0:1], s[78:79], 11
	v_writelane_b32 v253, s0, 52
	s_mov_b32 s89, s15
	s_nop 0
	v_writelane_b32 v253, s1, 53
	s_add_u32 s0, s82, s78
	s_addc_u32 s1, s15, s79
	v_writelane_b32 v253, s0, 54
	s_nop 1
	v_writelane_b32 v253, s1, 55
	s_lshl_b32 s0, s88, 8
	s_lshl_b32 s1, s78, 8
	v_writelane_b32 v253, s1, 56
	s_or_b32 s1, s0, 3
	v_writelane_b32 v253, s1, 57
	s_or_b32 s1, s0, 2
	v_writelane_b32 v253, s1, 58
	v_writelane_b32 v253, s0, 59
	s_or_b32 s0, s0, 1
	v_writelane_b32 v253, s0, 60
	s_add_i32 s0, 0, 0x224f0
	v_writelane_b32 v253, s0, 61
	s_add_i32 s0, 0, 0x22460
	v_writelane_b32 v253, s0, 62
	s_add_i32 s0, 0, 0x22470
	v_writelane_b32 v253, s0, 63
	s_add_i32 s0, 0, 0x22480
	v_writelane_b32 v254, s0, 0
	s_add_i32 s0, 0, 0x22490
	v_writelane_b32 v254, s0, 1
	s_add_i32 s0, 0, 0x2200
	v_writelane_b32 v254, s0, 2
	s_add_i32 s0, 0, 0x4200
	v_writelane_b32 v254, s0, 3
	s_add_i32 s0, 0, 0x22410
	v_writelane_b32 v254, s0, 4
	s_add_i32 s0, 0, 0x22420
	v_writelane_b32 v254, s0, 5
	s_add_i32 s0, 0, 0x224a8
	v_writelane_b32 v254, s0, 6
	s_add_i32 s0, 0, 0x224a0
	v_writelane_b32 v254, s0, 7
	s_add_i32 s0, 0, 0x22458
	v_writelane_b32 v254, s0, 8
	s_add_i32 s0, 0, 0x22440
	v_writelane_b32 v254, s0, 9
	s_add_i32 s0, 0, 0x22430
	v_writelane_b32 v254, s0, 10
	s_add_i32 s0, 0, 0x22400
	v_writelane_b32 v254, s0, 11
	s_add_i32 s0, 0, 0x224c0
	v_writelane_b32 v254, s0, 12
	s_add_i32 s0, 0, 0x22408
	v_writelane_b32 v254, s0, 13
	s_add_i32 s0, 0, 0x224d0
	v_writelane_b32 v254, s0, 14
	s_add_i32 s0, 0, 0x20014
	v_writelane_b32 v254, s0, 15
	s_add_i32 s0, 0, 0x20010
	v_writelane_b32 v254, s0, 16
	s_add_i32 s0, 0, 0x20008
	v_writelane_b32 v254, s0, 17
	s_add_i32 s0, 0, 0x20000
	v_writelane_b32 v254, s0, 18
	s_add_i32 s0, 0, 0x20004
	v_writelane_b32 v254, s0, 19
	s_add_i32 s0, 0, 0x224e0
	v_writelane_b32 v254, s0, 20
	s_add_i32 s0, 0, 0x22448
	v_writelane_b32 v254, s0, 21
	s_add_i32 s0, 0, 0x22450
	v_writelane_b32 v254, s0, 22
	s_add_i32 s0, 0, 0x22418
	v_writelane_b32 v254, s0, 23
	s_add_i32 s0, 0, 0x22498
	v_writelane_b32 v254, s0, 24
	s_add_i32 s0, 0, 0x224b0
	v_writelane_b32 v254, s0, 25
	s_add_i32 s0, 0, 0x224c8
	v_writelane_b32 v254, s0, 26
	s_add_i32 s0, 0, 0x20040
	v_writelane_b32 v254, s0, 27
	s_add_i32 s0, 0, 0x200c0
	v_writelane_b32 v254, s0, 28
	s_add_i32 s0, 0, 0x21400
	v_writelane_b32 v254, s0, 29
	s_add_i32 s0, 0, 0x21c00
	v_writelane_b32 v254, s0, 30
	s_add_i32 s0, 0, 0x20140
	v_writelane_b32 v254, s0, 31
	s_add_i32 s0, 0, 0x20200
	v_writelane_b32 v254, s0, 32
	s_add_i32 s0, 0, 0x20150
	v_writelane_b32 v254, s0, 33
	s_add_i32 s0, 0, 0x20210
	v_writelane_b32 v254, s0, 34
	s_add_i32 s0, 0, 0x20160
	v_writelane_b32 v254, s0, 35
	s_add_i32 s0, 0, 0x20220
	v_writelane_b32 v254, s0, 36
	s_add_i32 s0, 0, 0x20170
	v_writelane_b32 v254, s0, 37
	s_add_i32 s0, 0, 0x20230
	v_writelane_b32 v254, s0, 38
	s_add_i32 s0, 0, 0x20180
	v_writelane_b32 v254, s0, 39
	s_add_i32 s0, 0, 0x20240
	v_writelane_b32 v254, s0, 40
	s_add_i32 s0, 0, 0x20190
	v_writelane_b32 v254, s0, 41
	s_add_i32 s0, 0, 0x20250
	v_writelane_b32 v254, s0, 42
	s_add_i32 s0, 0, 0x201a0
	v_writelane_b32 v254, s0, 43
	s_add_i32 s0, 0, 0x20260
	v_writelane_b32 v254, s0, 44
	s_add_i32 s0, 0, 0x201b0
	v_writelane_b32 v254, s0, 45
	s_add_i32 s0, 0, 0x20270
	v_writelane_b32 v254, s0, 46
	s_add_i32 s0, 0, 0x201c0
	v_writelane_b32 v254, s0, 47
	s_add_i32 s0, 0, 0x20280
	v_writelane_b32 v254, s0, 48
	s_add_i32 s0, 0, 0x20144
	v_writelane_b32 v254, s0, 49
	s_add_i32 s0, 0, 0x2014c
	v_writelane_b32 v254, s0, 50
	s_add_i32 s0, 0, 0x20154
	v_writelane_b32 v254, s0, 51
	s_add_i32 s0, 0, 0x2015c
	v_writelane_b32 v254, s0, 52
	s_add_i32 s0, 0, 0x20164
	v_writelane_b32 v254, s0, 53
	s_add_i32 s0, 0, 0x2016c
	v_writelane_b32 v254, s0, 54
	s_add_i32 s0, 0, 0x20174
	v_writelane_b32 v254, s0, 55
	s_add_i32 s0, 0, 0x2017c
	v_writelane_b32 v254, s0, 56
	s_add_i32 s0, 0, 0x20184
	v_writelane_b32 v254, s0, 57
	s_add_i32 s0, 0, 0x2018c
	v_writelane_b32 v254, s0, 58
	s_add_i32 s0, 0, 0x20194
	v_writelane_b32 v254, s0, 59
	s_add_i32 s0, 0, 0x2019c
	v_writelane_b32 v254, s0, 60
	s_add_i32 s0, 0, 0x201a4
	v_writelane_b32 v254, s0, 61
	s_add_i32 s0, 0, 0x201ac
	v_writelane_b32 v254, s0, 62
	s_add_i32 s0, 0, 0x201b4
	v_writelane_b32 v254, s0, 63
	s_add_i32 s0, 0, 0x201bc
	v_writelane_b32 v255, s0, 0
	s_add_i32 s0, 0, 0x224e8
	v_writelane_b32 v255, s0, 1
	s_mov_b64 s[0:1], 0xc0000
	v_writelane_b32 v255, s0, 2
	s_nop 1
	v_writelane_b32 v255, s1, 3
	s_mov_b64 s[0:1], 0x400
	v_writelane_b32 v255, s0, 4
	s_nop 1
	v_writelane_b32 v255, s1, 5
	s_mov_b64 s[0:1], 0x408
	v_writelane_b32 v255, s0, 6
	s_nop 1
	v_writelane_b32 v255, s1, 7
	s_mov_b64 s[0:1], s[72:73]
	v_writelane_b32 v255, s0, 8
	s_nop 1
	v_writelane_b32 v255, s1, 9
	v_writelane_b32 v255, s2, 10
	v_writelane_b32 v255, s3, 11
	v_writelane_b32 v255, s56, 12
	s_nop 1
	v_writelane_b32 v255, s57, 13
	v_writelane_b32 v255, s82, 14
	v_writelane_b32 v255, s78, 15
	s_nop 1
	v_writelane_b32 v255, s79, 16
	v_writelane_b32 v255, s96, 17
	s_nop 1
	v_writelane_b32 v255, s97, 18
	v_writelane_b32 v255, s88, 19
	s_nop 1
	v_writelane_b32 v255, s89, 20
	v_writelane_b32 v255, s90, 21
	s_nop 1
	v_writelane_b32 v255, s91, 22
	v_writelane_b32 v255, s83, 23
	v_writelane_b32 v255, s89, 24
	v_writelane_b32 v255, s26, 25
	s_branch .LBB0_20

.LBB0_662:
	s_and_b64 vcc, exec, s[2:3]
	s_cbranch_vccnz .LBB0_806
	v_mov_b32_e32 v1, s15
	s_movk_i32 s0, 0xffc0
	v_bfi_b32 v1, s0, v1, v2
	s_mov_b32 s16, 0x4ec4ec4f
	v_mul_hi_i32 v5, v1, s16
	v_lshrrev_b32_e32 v6, 31, v5
	v_ashrrev_i32_e32 v5, 2, v5
	v_add_u32_e32 v5, v5, v6
	s_ashr_i32 s51, s15, 6
	v_mul_lo_u32 v6, v5, 13
	v_sub_u32_e32 v1, v1, v6
	s_lshl_b32 s36, s51, 10
	s_and_b32 s6, s15, 0xffffffc0
	v_cmp_gt_i32_e32 vcc, 8, v1
	v_cmp_eq_u32_e64 s[0:1], 12, v1
	s_add_i32 s38, s36, 0
	s_or_b64 s[4:5], vcc, s[0:1]
	s_add_i32 s7, s6, 0x200
	s_add_i32 s37, s38, 0x15000
	s_add_i32 s14, s38, 0x2000
	v_lshlrev_b32_e32 v1, 3, v1
	s_cmp_lt_i32 s51, 5
	v_add_u32_e32 v6, 0x3c0, v1
	s_cselect_b64 s[12:13], -1, 0
	s_movk_i32 s17, 0x420
	v_cndmask_b32_e64 v6, v6, 0, s[0:1]
	s_and_b64 s[0:1], s[12:13], exec
	v_and_b32_e32 v4, 63, v2
	v_mul_lo_u32 v5, v5, s17
	v_cndmask_b32_e32 v1, v6, v1, vcc
	s_cselect_b32 s0, s7, s6
	v_add_lshl_u32 v1, v1, v5, 1
	v_or_b32_e32 v5, s0, v4
	v_mul_hi_i32 v6, v5, s16
	v_lshrrev_b32_e32 v7, 31, v6
	v_ashrrev_i32_e32 v6, 2, v6
	v_add_u32_e32 v6, v6, v7
	v_mul_lo_u32 v7, v6, 13
	v_sub_u32_e32 v5, v5, v7
	v_cmp_gt_i32_e32 vcc, 8, v5
	v_cmp_eq_u32_e64 s[0:1], 12, v5
	v_lshlrev_b32_e32 v5, 3, v5
	v_add_u32_e32 v7, 0x3c0, v5
	v_cndmask_b32_e64 v7, v7, 0, s[0:1]
	s_cselect_b32 s14, s14, s37
	s_or_b64 s[6:7], vcc, s[0:1]
	v_mul_lo_u32 v6, v6, s17
	v_cndmask_b32_e32 v5, v7, v5, vcc
	s_and_b32 s0, s15, 0xc0
	v_add_lshl_u32 v181, v5, v6, 1
	v_or_b32_e32 v5, s0, v4
	s_ashr_i32 s0, s15, 3
	s_and_b32 s0, s0, 0x7fffffe0
	v_lshrrev_b32_e32 v5, 2, v5
	v_mov_b32_e32 v6, s0
	v_mad_u32_u24 v5, v5, s17, v6
	v_lshlrev_b32_e32 v6, 3, v2
	v_and_or_b32 v5, v6, 24, v5
	v_readlane_b32 s0, v252, 20
	v_lshlrev_b32_e32 v198, 1, v5
	s_add_i32 s57, s33, -1
	v_mov_b32_e32 v5, s0
	v_cndmask_b32_e64 v6, 0, v5, s[4:5]
	v_cndmask_b32_e64 v5, 0, v5, s[6:7]
	v_add_u32_e32 v200, v6, v1
	v_add_u32_e32 v201, v5, v181
	s_add_i32 s0, s38, 0x3400
	s_mov_b32 s1, m0
	s_mov_b32 m0, s38
	s_nop 0
	global_load_lds_dwordx4 v200, s[8:9]
	s_mov_b32 m0, s14
	s_or_b64 exec, s[12:13], 1
	global_load_lds_dwordx4 v201, s[8:9]
	s_mov_b64 exec, -1
	s_mov_b32 m0, s0
	s_nop 0
	global_load_lds_dwordx4 v198, s[10:11]
	s_mov_b32 m0, s1
	s_mov_b64 s[20:21], -1
	s_cmp_lg_u32 s57, 0
	s_mov_b64 s[0:1], -1
	s_cbranch_scc0 .LBB0_665
	s_add_u32 s16, s8, 0x21000
	s_addc_u32 s17, s9, 0
	s_add_u32 s18, s10, 0x21000
	s_addc_u32 s19, s11, 0
	s_mov_b64 s[0:1], 0

.LBB0_671:
	s_add_i32 s10, s38, 0x5400
	s_add_i32 s11, s38, 0x7400
	s_and_b64 s[8:9], s[12:13], exec
	s_cselect_b32 s8, s11, s37
	s_add_i32 s9, s38, 0x8800
	s_mov_b32 s11, m0
	s_mov_b32 m0, s10
	s_nop 0
	global_load_lds_dwordx4 v200, s[16:17]
	s_mov_b32 m0, s8
	s_or_b64 exec, s[12:13], 1
	global_load_lds_dwordx4 v201, s[16:17]
	s_mov_b64 exec, -1
	s_mov_b32 m0, s9
	s_nop 0
	global_load_lds_dwordx4 v198, s[18:19]
	s_mov_b32 m0, s11
	s_andn2_b64 vcc, exec, s[20:21]
	s_mov_b64 s[20:21], 0
	s_cbranch_vccnz .LBB0_679
	s_add_i32 s57, s57, -1
	s_mov_b64 s[8:9], -1
	s_cmp_lg_u32 s57, 0
	s_mov_b64 s[24:25], -1
	s_cbranch_scc0 .LBB0_674
	s_add_u32 s10, s16, 0x21000
	s_addc_u32 s11, s17, 0
	s_add_u32 s22, s18, 0x21000
	s_addc_u32 s23, s19, 0
	s_mov_b64 s[24:25], 0
.LBB0_674:
	s_andn2_b64 vcc, exec, s[24:25]
	s_cbranch_vccnz .LBB0_680
	s_add_i32 s10, s54, 1
	s_mul_i32 s11, s10, s78
	s_add_i32 s11, s11, s39
	s_cmpk_lt_i32 s11, 0x800
	s_cselect_b64 s[8:9], -1, 0
	s_cmpk_gt_i32 s11, 0x7ff
	s_mov_b32 s55, s40
	s_cbranch_scc1 .LBB0_677
	s_lshl_b32 s1, s11, 5
	s_and_b32 s1, s1, 0xf00
	s_bfe_u32 s0, s11, 0x40007
	s_sub_i32 s1, 0x1000, s1
	s_ashr_i32 s55, s1, 6
	s_mul_i32 s0, s0, 0x840000
	s_add_u32 s0, s27, s0
	s_addc_u32 s1, s26, 0
	s_add_u32 s0, s0, 0x20e00000
	s_addc_u32 s1, s1, 0
	s_lshl_b32 s11, s11, 8
	s_and_b32 s56, s11, 0x700
	s_add_u32 s11, s0, s56
	s_addc_u32 s15, s1, 0
	s_add_u32 s14, s11, 0x80
	s_addc_u32 s15, s15, 0

.LBB0_682:
	s_add_i32 s22, s38, 0xa800
	s_add_i32 s23, s38, 0xc800
	s_and_b64 s[10:11], s[12:13], exec
	s_cselect_b32 s10, s23, s37
	s_add_i32 s38, s38, 0xdc00
	s_andn2_b64 vcc, exec, s[8:9]
	s_mov_b32 s8, m0
	s_mov_b32 m0, s22
	s_nop 0
	global_load_lds_dwordx4 v200, s[16:17]
	s_mov_b32 m0, s10
	s_or_b64 exec, s[12:13], 1
	global_load_lds_dwordx4 v201, s[16:17]
	s_mov_b64 exec, -1
	s_mov_b32 m0, s38
	s_nop 0
	global_load_lds_dwordx4 v198, s[18:19]
	s_mov_b32 m0, s8
	s_cbranch_vccnz .LBB0_692
	s_add_i32 s57, s57, -1
	s_mov_b64 s[20:21], -1
	s_cmp_lg_u32 s57, 0
	s_mov_b64 s[22:23], -1
	s_cbranch_scc0 .LBB0_685
	s_add_u32 s8, s16, 0x21000
	s_addc_u32 s9, s17, 0
	s_add_u32 s10, s18, 0x21000
	s_addc_u32 s11, s19, 0
	s_mov_b64 s[22:23], 0
.LBB0_685:
	s_andn2_b64 vcc, exec, s[22:23]
	s_cbranch_vccnz .LBB0_690
	s_add_i32 s10, s54, 1
	s_bitcmp0_b32 s54, 0
	v_readlane_b32 s9, v252, 25
	s_mul_i32 s8, s10, s78
	s_cselect_b32 s11, s9, s82
	s_add_i32 s11, s11, s8
	s_cmpk_lt_i32 s11, 0x800
	s_cselect_b64 s[8:9], -1, 0
	s_cmpk_gt_i32 s11, 0x7ff
	s_cbranch_scc1 .LBB0_688
	s_lshl_b32 s1, s11, 5
	s_and_b32 s1, s1, 0xf00
	s_bfe_u32 s0, s11, 0x40007
	s_sub_i32 s1, 0x1000, s1
	s_ashr_i32 s55, s1, 6
	s_mul_i32 s0, s0, 0x840000
	s_add_u32 s0, s27, s0
	s_addc_u32 s1, s26, 0
	s_add_u32 s0, s0, 0x20e00000
	s_addc_u32 s1, s1, 0
	s_lshl_b32 s11, s11, 8
	s_and_b32 s56, s11, 0x700
	s_add_u32 s11, s0, s56
	s_addc_u32 s15, s1, 0
	s_add_u32 s14, s11, 0x80
	s_addc_u32 s15, s15, 0

.LBB0_696:
	s_mul_i32 s10, s60, 0x5400
	s_add_i32 s26, s10, 0
	s_add_i32 s27, s26, s36
	s_add_i32 s28, s26, s59
	s_and_b64 s[10:11], s[12:13], exec
	s_cselect_b32 s10, s28, s37
	s_add_i32 s11, s26, s58
	s_mov_b32 s26, m0
	s_mov_b32 m0, s27
	s_nop 0
	global_load_lds_dwordx4 v200, s[16:17]
	s_mov_b32 m0, s10
	s_or_b64 exec, s[12:13], 1
	global_load_lds_dwordx4 v201, s[16:17]
	s_mov_b64 exec, -1
	s_mov_b32 m0, s11
	s_nop 0
	global_load_lds_dwordx4 v198, s[18:19]
	s_mov_b32 m0, s26
	s_andn2_b64 vcc, exec, s[20:21]
	s_mov_b64 s[20:21], 0
	s_cbranch_vccnz .LBB0_706
	s_add_i32 s57, s57, -1
	s_mov_b64 s[20:21], -1
	s_cmp_lg_u32 s57, 0
	s_mov_b64 s[28:29], -1
	s_cbranch_scc0 .LBB0_699
	s_add_u32 s10, s16, 0x21000
	s_addc_u32 s11, s17, 0
	s_add_u32 s26, s18, 0x21000
	s_addc_u32 s27, s19, 0
	s_mov_b64 s[28:29], 0
.LBB0_699:
	s_andn2_b64 vcc, exec, s[28:29]
	s_cbranch_vccnz .LBB0_704
	s_add_i32 s26, s54, 1
	s_bitcmp0_b32 s54, 0
	v_readlane_b32 s11, v252, 25
	s_mul_i32 s10, s26, s78
	s_cselect_b32 s20, s11, s82
	s_add_i32 s20, s20, s10
	s_cmpk_lt_i32 s20, 0x800
	s_cselect_b64 s[10:11], -1, 0
	s_cmpk_gt_i32 s20, 0x7ff
	s_cbranch_scc1 .LBB0_702
	s_lshl_b32 s1, s20, 5
	s_and_b32 s1, s1, 0xf00
	s_bfe_u32 s0, s20, 0x40007
	s_sub_i32 s1, 0x1000, s1
	s_ashr_i32 s55, s1, 6
	s_mul_i32 s0, s0, 0x840000
	s_add_u32 s0, s62, s0
	s_addc_u32 s1, s63, 0
	s_lshl_b32 s14, s20, 8
	s_and_b32 s56, s14, 0x700
	s_add_u32 s14, s0, s56
	s_addc_u32 s15, s1, 0
	s_add_u32 s14, s14, 0x80
	s_addc_u32 s15, s15, 0

.LBB0_745:
	s_mul_i32 s10, s60, 0x5400
	s_add_i32 s26, s10, 0
	s_add_i32 s27, s26, s36
	s_add_i32 s28, s26, s59
	s_and_b64 s[10:11], s[12:13], exec
	s_cselect_b32 s10, s28, s37
	s_add_i32 s11, s26, s58
	s_mov_b32 s26, m0
	s_mov_b32 m0, s27
	s_nop 0
	global_load_lds_dwordx4 v200, s[16:17]
	s_mov_b32 m0, s10
	s_or_b64 exec, s[12:13], 1
	global_load_lds_dwordx4 v201, s[16:17]
	s_mov_b64 exec, -1
	s_mov_b32 m0, s11
	s_nop 0
	global_load_lds_dwordx4 v198, s[18:19]
	s_mov_b32 m0, s26
	s_andn2_b64 vcc, exec, s[20:21]
	s_mov_b64 s[10:11], 0
	s_cbranch_vccnz .LBB0_753
	s_add_i32 s57, s57, -1
	s_mov_b64 s[20:21], -1
	s_cmp_lg_u32 s57, 0
	s_mov_b64 s[30:31], -1
	s_cbranch_scc0 .LBB0_748
	s_add_u32 s26, s16, 0x21000
	s_addc_u32 s27, s17, 0
	s_add_u32 s28, s18, 0x21000
	s_addc_u32 s29, s19, 0
	s_mov_b64 s[30:31], 0
.LBB0_748:
	s_andn2_b64 vcc, exec, s[30:31]
	s_cbranch_vccnz .LBB0_754
	s_add_i32 s26, s54, 1
	s_bitcmp0_b32 s54, 0
	v_readlane_b32 s21, v252, 25
	s_mul_i32 s20, s26, s78
	s_cselect_b32 s27, s21, s82
	s_add_i32 s27, s27, s20
	s_cmpk_lt_i32 s27, 0x800
	s_cselect_b64 s[20:21], -1, 0
	s_cmpk_gt_i32 s27, 0x7ff
	s_cbranch_scc1 .LBB0_751
	s_lshl_b32 s1, s27, 5
	s_and_b32 s1, s1, 0xf00
	s_bfe_u32 s0, s27, 0x40007
	s_sub_i32 s1, 0x1000, s1
	s_ashr_i32 s55, s1, 6
	s_mul_i32 s0, s0, 0x840000
	s_add_u32 s0, s62, s0
	s_addc_u32 s1, s63, 0
	s_lshl_b32 s14, s27, 8
	s_and_b32 s56, s14, 0x700
	s_add_u32 s14, s0, s56
	s_addc_u32 s15, s1, 0
	s_add_u32 s14, s14, 0x80
	s_addc_u32 s15, s15, 0

.LBB0_766:
	v_and_b32_e32 v2, 64, v242
	v_xor_b32_e32 v4, 32, v242
	v_add_u32_e32 v2, 64, v2
	v_cmp_lt_i32_e32 vcc, v4, v2
	s_movk_i32 s26, 0xc00
	s_lshl_b32 s92, s65, 7
	v_cndmask_b32_e32 v4, v242, v4, vcc
	v_lshlrev_b32_e32 v50, 2, v4
	ds_bpermute_b32 v4, v50, v191
	v_mov_b32_e32 v193, v3
	s_movk_i32 s84, 0xc00
	s_waitcnt lgkmcnt(0)
	v_add_f32_e32 v4, v191, v4
	v_div_scale_f32 v5, s[10:11], v4, v4, 1.0
	v_rcp_f32_e32 v6, v5
	v_div_scale_f32 v7, vcc, 1.0, v4, 1.0
	v_fma_f32 v8, -v5, v6, 1.0
	v_fmac_f32_e32 v6, v8, v6
	v_mul_f32_e32 v8, v7, v6
	v_fma_f32 v9, -v5, v8, v7
	v_fmac_f32_e32 v8, v9, v6
	v_fma_f32 v5, -v5, v8, v7
	v_div_fmas_f32 v5, v5, v6, v8
	v_div_fixup_f32 v4, v5, v4, 1.0
	v_pk_mul_f32 v[6:7], v[34:35], v[4:5] op_sel_hi:[1,0]
	v_pk_mul_f32 v[8:9], v[18:19], v[4:5] op_sel_hi:[1,0]
	v_pk_mul_f32 v[10:11], v[36:37], v[4:5] op_sel_hi:[1,0]
	v_pk_mul_f32 v[12:13], v[20:21], v[4:5] op_sel_hi:[1,0]
	v_pk_mul_f32 v[14:15], v[38:39], v[4:5] op_sel_hi:[1,0]
	v_pk_mul_f32 v[16:17], v[22:23], v[4:5] op_sel_hi:[1,0]
	v_pk_mul_f32 v[18:19], v[40:41], v[4:5] op_sel_hi:[1,0]
	v_pk_mul_f32 v[20:21], v[24:25], v[4:5] op_sel_hi:[1,0]
	v_pk_mul_f32 v[22:23], v[42:43], v[4:5] op_sel_hi:[1,0]
	v_pk_mul_f32 v[24:25], v[26:27], v[4:5] op_sel_hi:[1,0]
	v_pk_mul_f32 v[26:27], v[44:45], v[4:5] op_sel_hi:[1,0]
	v_pk_mul_f32 v[28:29], v[28:29], v[4:5] op_sel_hi:[1,0]
	v_pk_mul_f32 v[34:35], v[46:47], v[4:5] op_sel_hi:[1,0]
	v_pk_mul_f32 v[30:31], v[30:31], v[4:5] op_sel_hi:[1,0]
	v_pk_mul_f32 v[36:37], v[48:49], v[4:5] op_sel_hi:[1,0]
	v_pk_mul_f32 v[4:5], v[32:33], v[4:5] op_sel_hi:[1,0]
	v_mov_b64_e32 v[32:33], s[24:25]
	v_mad_u64_u32 v[32:33], s[10:11], v202, s26, v[32:33]
	v_mov_b32_e32 v38, v33
	v_mad_u64_u32 v[38:39], s[10:11], v203, s26, v[38:39]
	v_mov_b32_e32 v33, v38
	v_lshl_add_u64 v[32:33], v[32:33], 0, s[92:93]
	v_lshl_add_u64 v[32:33], v[32:33], 0, v[192:193]
	v_cvt_pk_bf16_f32 v6, v6, v7
	v_cvt_pk_bf16_f32 v7, v10, v11
	global_store_dwordx2 v[32:33], v[6:7], off
	v_cvt_pk_bf16_f32 v6, v14, v15
	v_cvt_pk_bf16_f32 v7, v18, v19
	s_add_i32 s26, s69, 1
	global_store_dwordx2 v[32:33], v[6:7], off offset:16
	v_cvt_pk_bf16_f32 v6, v22, v23
	v_cvt_pk_bf16_f32 v7, v26, v27
	s_bitcmp0_b32 s69, 0
	v_readlane_b32 s11, v252, 25
	global_store_dwordx2 v[32:33], v[6:7], off offset:32
	v_cvt_pk_bf16_f32 v6, v34, v35
	v_cvt_pk_bf16_f32 v7, v36, v37
	s_mul_i32 s10, s26, s78
	s_cselect_b32 s27, s11, s82
	global_store_dwordx2 v[32:33], v[6:7], off offset:48
	v_cvt_pk_bf16_f32 v6, v8, v9
	v_cvt_pk_bf16_f32 v7, v12, v13
	s_add_i32 s27, s27, s10
	global_store_dwordx2 v[32:33], v[6:7], off offset:64
	v_cvt_pk_bf16_f32 v6, v16, v17
	v_cvt_pk_bf16_f32 v7, v20, v21
	s_cmpk_gt_i32 s27, 0x7ff
	global_store_dwordx2 v[32:33], v[6:7], off offset:80
	v_cvt_pk_bf16_f32 v6, v24, v25
	v_cvt_pk_bf16_f32 v7, v28, v29
	s_cselect_b64 s[10:11], -1, 0
	global_store_dwordx2 v[32:33], v[6:7], off offset:96
	v_cvt_pk_bf16_f32 v6, v30, v31
	v_cvt_pk_bf16_f32 v7, v4, v5
	s_and_b64 vcc, exec, s[10:11]
	global_store_dwordx2 v[32:33], v[6:7], off offset:112
	s_cbranch_vccnz .LBB0_768
	s_bfe_u32 s66, s27, 0x40007
	s_and_b32 s65, s27, 7
	s_lshl_b32 s27, s27, 5
	s_and_b32 s27, s27, 0xf00
	s_sub_i32 s67, 0xf00, s27
	s_sub_i32 s27, 0x1000, s27
	s_ashr_i32 s33, s27, 6

.LBB0_806:
	v_readlane_b32 s0, v253, 61
	v_mov_b32_e32 v2, v232
	s_and_b64 vcc, exec, s[2:3]
	v_mov_b32_e32 v1, s0
	v_readlane_b32 s0, v254, 21
	s_waitcnt vmcnt(0)
	ds_read_b64 v[4:5], v1
	v_readfirstlane_b32 s4, v2
	v_mov_b32_e32 v1, s0
	ds_read_b64 v[6:7], v1
	s_waitcnt lgkmcnt(1)
	v_readfirstlane_b32 s15, v5
	v_readfirstlane_b32 s14, v4
	s_waitcnt lgkmcnt(0)
	v_readfirstlane_b32 s1, v7
	v_readfirstlane_b32 s0, v6
	s_cbranch_vccnz .LBB0_915
	v_mov_b32_e32 v1, s4
	s_movk_i32 s2, 0xffc0
	s_ashr_i32 s8, s4, 6
	v_bfi_b32 v1, s2, v1, v2
	s_ashr_i32 s2, s4, 3
	s_and_b32 s11, s2, 0x7fffffe0
	s_lshl_b32 s81, s8, 10
	s_mov_b32 s2, s76
	s_and_b32 s6, s4, 0xffffffc0
	s_add_i32 s9, s81, 0
	v_writelane_b32 v255, s2, 27
	s_lshl_b32 s92, s76, 7
	s_add_i32 s7, s6, 0x200
	s_and_b32 s10, s4, 0xc0
	s_add_i32 s71, s9, 0x11000
	v_writelane_b32 v255, s3, 28
	s_lshl_b64 s[2:3], s[92:93], 2
	s_add_u32 s0, s0, s2
	s_addc_u32 s1, s1, s3
	s_add_u32 s4, s14, 0xae00000
	v_writelane_b32 v255, s14, 29
	s_addc_u32 s5, s15, 0
	v_readlane_b32 s2, v252, 27
	v_writelane_b32 v255, s15, 30
	s_add_u32 s2, s4, s2
	v_writelane_b32 v255, s4, 31
	s_addc_u32 s3, s5, 0
	s_mov_b32 s12, 0x38e38e39
	v_writelane_b32 v255, s5, 32
	v_readlane_b32 s4, v252, 29
	s_add_u32 s2, s2, s4
	s_addc_u32 s3, s3, 0
	s_add_u32 s14, s2, 0x400
	v_mul_hi_i32 v4, v1, s12
	s_addc_u32 s15, s3, 0
	v_lshrrev_b32_e32 v5, 31, v4
	v_ashrrev_i32_e32 v4, 1, v4
	s_add_u32 s78, s2, 0x800
	v_add_u32_e32 v4, v4, v5
	s_addc_u32 s79, s3, 0
	s_add_i32 s2, s9, 0x2000
	v_lshl_add_u32 v5, v4, 3, v4
	s_cmp_lt_i32 s8, 1
	v_sub_u32_e32 v1, v1, v5
	s_cselect_b64 s[96:97], -1, 0
	v_cmp_gt_i32_e32 vcc, 8, v1
	v_lshlrev_b32_e32 v1, 4, v1
	s_and_b64 s[4:5], s[96:97], exec
	v_and_b32_e32 v132, 63, v2
	v_cndmask_b32_e32 v1, 0, v1, vcc
	s_cselect_b32 s3, s7, s6
	v_lshl_add_u32 v1, v4, 12, v1
	v_or_b32_e32 v4, s3, v132
	v_mul_hi_i32 v5, v4, s12
	v_lshrrev_b32_e32 v6, 31, v5
	v_ashrrev_i32_e32 v5, 1, v5
	v_add_u32_e32 v5, v5, v6
	v_lshl_add_u32 v6, v5, 3, v5
	v_sub_u32_e32 v4, v4, v6
	v_cmp_gt_i32_e32 vcc, 8, v4
	v_lshlrev_b32_e32 v4, 4, v4
	s_mov_b32 s13, s93
	v_cndmask_b32_e32 v4, 0, v4, vcc
	v_lshl_add_u32 v198, v5, 12, v4
	v_or_b32_e32 v4, s10, v132
	v_lshlrev_b32_e32 v4, 9, v4
	v_and_b32_e32 v4, 0x1f800, v4
	v_add_u32_e32 v4, s11, v4
	v_lshlrev_b32_e32 v5, 3, v2
	v_and_or_b32 v133, v5, 24, v4
	global_load_dwordx4 v[52:55], v3, s[0:1] offset:48
	global_load_dwordx4 v[84:87], v3, s[0:1] offset:32
	global_load_dwordx4 v[100:103], v3, s[0:1] offset:16
	global_load_dwordx4 v[116:119], v3, s[0:1]
	global_load_dwordx4 v[60:63], v3, s[0:1] offset:176
	global_load_dwordx4 v[88:91], v3, s[0:1] offset:160
	global_load_dwordx4 v[104:107], v3, s[0:1] offset:144
	global_load_dwordx4 v[120:123], v3, s[0:1] offset:128
	global_load_dwordx4 v[64:67], v3, s[0:1] offset:304
	global_load_dwordx4 v[92:95], v3, s[0:1] offset:288
	global_load_dwordx4 v[108:111], v3, s[0:1] offset:272
	global_load_dwordx4 v[124:127], v3, s[0:1] offset:256
	global_load_dwordx4 v[76:79], v3, s[0:1] offset:432
	global_load_dwordx4 v[96:99], v3, s[0:1] offset:416
	global_load_dwordx4 v[112:115], v3, s[0:1] offset:400
	global_load_dwordx4 v[128:131], v3, s[0:1] offset:384
	global_load_dwordx4 v[4:7], v3, s[0:1] offset:112
	global_load_dwordx4 v[20:23], v3, s[0:1] offset:96
	global_load_dwordx4 v[36:39], v3, s[0:1] offset:80
	global_load_dwordx4 v[56:59], v3, s[0:1] offset:64
	global_load_dwordx4 v[8:11], v3, s[0:1] offset:240
	global_load_dwordx4 v[24:27], v3, s[0:1] offset:224
	global_load_dwordx4 v[40:43], v3, s[0:1] offset:208
	global_load_dwordx4 v[68:71], v3, s[0:1] offset:192
	global_load_dwordx4 v[12:15], v3, s[0:1] offset:368
	global_load_dwordx4 v[28:31], v3, s[0:1] offset:352
	global_load_dwordx4 v[44:47], v3, s[0:1] offset:336
	global_load_dwordx4 v[72:75], v3, s[0:1] offset:320
	global_load_dwordx4 v[16:19], v3, s[0:1] offset:496
	global_load_dwordx4 v[32:35], v3, s[0:1] offset:480
	global_load_dwordx4 v[48:51], v3, s[0:1] offset:464
	global_load_dwordx4 v[80:83], v3, s[0:1] offset:448
	s_cselect_b32 s0, s2, s71
	v_lshlrev_b32_e32 v199, 1, v133
	s_add_i32 s1, s9, 0x2400
	s_mov_b32 s2, m0
	s_mov_b32 m0, s9
	s_nop 0
	global_load_lds_dwordx4 v1, s[14:15]
	s_mov_b32 m0, s0
	s_or_b64 exec, s[96:97], 1
	global_load_lds_dwordx4 v198, s[14:15]
	s_mov_b64 exec, -1
	s_mov_b32 m0, s1
	s_nop 0
	global_load_lds_dwordx4 v199, s[78:79]
	s_mov_b32 m0, s2
	v_readlane_b32 s0, v252, 19
	s_add_i32 s69, s0, -1
	s_mov_b64 s[0:1], -1
	s_cmp_lg_u32 s69, 0
	s_mov_b64 s[2:3], -1
	s_cbranch_scc0 .LBB0_809
	s_add_u32 s92, s14, 0x40000
	s_addc_u32 s93, s15, 0
	s_add_u32 s76, s78, 0x40000
	s_addc_u32 s77, s79, 0
	s_mov_b64 s[2:3], 0

.LBB0_814:
	s_add_i32 s4, s9, 0x4400
	s_add_i32 s5, s9, 0x6400
	s_and_b64 s[2:3], s[96:97], exec
	s_cselect_b32 s2, s5, s71
	s_add_i32 s3, s9, 0x6800
	s_mov_b32 s5, m0
	s_mov_b32 m0, s4
	s_nop 0
	global_load_lds_dwordx4 v1, s[92:93]
	s_mov_b32 m0, s2
	s_or_b64 exec, s[96:97], 1
	global_load_lds_dwordx4 v198, s[92:93]
	s_mov_b64 exec, -1
	s_mov_b32 m0, s3
	s_nop 0
	global_load_lds_dwordx4 v199, s[76:77]
	s_mov_b32 m0, s5
	v_writelane_b32 v255, s14, 33
	s_andn2_b64 vcc, exec, s[0:1]
	s_mov_b64 s[72:73], 0
	v_writelane_b32 v255, s15, 34
	s_cbranch_vccnz .LBB0_822
	s_add_i32 s69, s69, -1
	s_mov_b64 s[0:1], -1
	s_cmp_lg_u32 s69, 0
	s_mov_b64 s[6:7], -1
	s_cbranch_scc0 .LBB0_817
	s_add_u32 s2, s92, 0x40000
	s_addc_u32 s3, s93, 0
	s_add_u32 s4, s76, 0x40000
	s_addc_u32 s5, s77, 0
	s_mov_b64 s[6:7], 0
.LBB0_817:
	s_andn2_b64 vcc, exec, s[6:7]
	s_cbranch_vccnz .LBB0_823
	s_add_i32 s2, s90, 1
	v_readlane_b32 s0, v255, 15
	s_mul_i32 s3, s2, s0
	s_add_i32 s3, s3, s10
	v_readlane_b32 s1, v255, 16
	s_cmpk_lt_i32 s3, 0x800
	s_cselect_b64 s[0:1], -1, 0
	s_cmpk_gt_i32 s3, 0x7ff
	s_cbranch_scc1 .LBB0_820
	s_lshl_b32 s4, s3, 5
	s_and_b32 s4, s4, 0xf00
	s_sub_i32 s4, 0x1000, s4
	s_ashr_i32 s16, s4, 6
	s_lshl_b32 s4, s3, 17
	s_and_b32 s4, s4, 0xf000000
	v_readlane_b32 s6, v255, 31
	v_readlane_b32 s7, v255, 32
	s_add_u32 s4, s6, s4
	s_addc_u32 s5, s7, 0
	s_lshl_b32 s3, s3, 7
	s_and_b32 s3, s3, 0x380
	s_add_u32 s3, s4, s3
	s_addc_u32 s4, s5, 0
	s_add_u32 s6, s3, 0x400
	s_addc_u32 s7, s4, 0
	v_writelane_b32 v255, s6, 33
	s_add_u32 s78, s3, 0x800
	s_addc_u32 s79, s4, 0
	v_writelane_b32 v255, s7, 34

.LBB0_825:
	s_add_i32 s4, s9, 0x8800
	s_add_i32 s5, s9, 0xa800
	s_and_b64 s[2:3], s[96:97], exec
	s_cselect_b32 s2, s5, s71
	s_add_i32 s9, s9, 0xac00
	s_andn2_b64 vcc, exec, s[0:1]
	s_mov_b32 s0, m0
	s_mov_b32 m0, s4
	s_nop 0
	global_load_lds_dwordx4 v1, s[92:93]
	s_mov_b32 m0, s2
	s_or_b64 exec, s[96:97], 1
	global_load_lds_dwordx4 v198, s[92:93]
	s_mov_b64 exec, -1
	s_mov_b32 m0, s9
	s_nop 0
	global_load_lds_dwordx4 v199, s[76:77]
	s_mov_b32 m0, s0
	s_cbranch_vccnz .LBB0_835
	s_add_i32 s69, s69, -1
	s_mov_b64 s[72:73], -1
	s_cmp_lg_u32 s69, 0
	s_mov_b64 s[4:5], -1
	s_cbranch_scc0 .LBB0_828
	s_add_u32 s0, s92, 0x40000
	s_addc_u32 s1, s93, 0
	s_add_u32 s2, s76, 0x40000
	s_addc_u32 s3, s77, 0
	s_mov_b64 s[4:5], 0
.LBB0_828:
	s_andn2_b64 vcc, exec, s[4:5]
	s_cbranch_vccnz .LBB0_833
	v_readlane_b32 s0, v255, 15
	s_add_i32 s2, s90, 1
	v_readlane_b32 s1, v255, 16
	s_bitcmp0_b32 s90, 0
	v_readlane_b32 s1, v252, 25
	s_mul_i32 s0, s2, s0
	s_cselect_b32 s3, s1, s82
	s_add_i32 s3, s3, s0
	s_cmpk_lt_i32 s3, 0x800
	s_cselect_b64 s[0:1], -1, 0
	s_cmpk_gt_i32 s3, 0x7ff
	s_cbranch_scc1 .LBB0_831
	s_lshl_b32 s4, s3, 5
	s_and_b32 s4, s4, 0xf00
	s_sub_i32 s4, 0x1000, s4
	s_ashr_i32 s16, s4, 6
	s_lshl_b32 s4, s3, 17
	s_and_b32 s4, s4, 0xf000000
	v_readlane_b32 s6, v255, 31
	v_readlane_b32 s7, v255, 32
	s_add_u32 s4, s6, s4
	s_addc_u32 s5, s7, 0
	s_lshl_b32 s3, s3, 7
	s_and_b32 s3, s3, 0x380
	s_add_u32 s3, s4, s3
	s_addc_u32 s4, s5, 0
	s_add_u32 s6, s3, 0x400
	s_addc_u32 s7, s4, 0
	v_writelane_b32 v255, s6, 33
	s_add_u32 s78, s3, 0x800
	s_addc_u32 s79, s4, 0
	v_writelane_b32 v255, s7, 34

.LBB0_840:
	s_mul_i32 s0, s91, 0x4400
	s_add_i32 s2, s0, 0
	s_add_i32 s3, s2, s81
	s_add_i32 s4, s2, s33
	s_and_b64 s[0:1], s[96:97], exec
	s_cselect_b32 s0, s4, s71
	s_add_i32 s1, s2, s70
	s_mov_b32 s2, m0
	s_mov_b32 m0, s3
	s_nop 0
	global_load_lds_dwordx4 v1, s[92:93]
	s_mov_b32 m0, s0
	s_or_b64 exec, s[96:97], 1
	global_load_lds_dwordx4 v198, s[92:93]
	s_mov_b64 exec, -1
	s_mov_b32 m0, s1
	s_nop 0
	global_load_lds_dwordx4 v199, s[76:77]
	s_mov_b32 m0, s2
	s_andn2_b64 vcc, exec, s[72:73]
	s_mov_b64 s[0:1], 0
	s_cbranch_vccnz .LBB0_848
	s_add_i32 s69, s69, -1
	s_mov_b64 s[72:73], -1
	s_cmp_lg_u32 s69, 0
	s_mov_b64 s[6:7], -1
	s_cbranch_scc0 .LBB0_843
	s_add_u32 s2, s92, 0x40000
	s_addc_u32 s3, s93, 0
	s_add_u32 s4, s76, 0x40000
	s_addc_u32 s5, s77, 0
	s_mov_b64 s[6:7], 0
.LBB0_843:
	s_andn2_b64 vcc, exec, s[6:7]
	s_cbranch_vccnz .LBB0_849
	v_readlane_b32 s2, v255, 15
	s_add_i32 s4, s90, 1
	v_readlane_b32 s3, v255, 16
	s_bitcmp0_b32 s90, 0
	v_readlane_b32 s3, v252, 25
	s_mul_i32 s2, s4, s2
	s_cselect_b32 s5, s3, s82
	s_add_i32 s5, s5, s2
	s_cmpk_lt_i32 s5, 0x800
	s_cselect_b64 s[2:3], -1, 0
	s_cmpk_gt_i32 s5, 0x7ff
	s_cbranch_scc1 .LBB0_846
	s_lshl_b32 s6, s5, 5
	s_and_b32 s6, s6, 0xf00
	s_sub_i32 s6, 0x1000, s6
	s_ashr_i32 s16, s6, 6
	s_lshl_b32 s6, s5, 17
	s_and_b32 s6, s6, 0xf000000
	v_readlane_b32 s12, v255, 31
	v_readlane_b32 s13, v255, 32
	s_add_u32 s6, s12, s6
	s_addc_u32 s7, s13, 0
	s_lshl_b32 s5, s5, 7
	s_and_b32 s5, s5, 0x380
	s_add_u32 s5, s6, s5
	s_addc_u32 s6, s7, 0
	s_add_u32 s12, s5, 0x400
	s_addc_u32 s13, s6, 0
	v_writelane_b32 v255, s12, 33
	s_add_u32 s78, s5, 0x800
	s_addc_u32 s79, s6, 0
	v_writelane_b32 v255, s13, 34

.LBB0_874:
	s_andn2_b64 vcc, exec, s[6:7]
	s_cbranch_vccnz .LBB0_880
	v_readlane_b32 s2, v255, 15
	s_add_i32 s4, s90, 1
	v_readlane_b32 s3, v255, 16
	s_bitcmp0_b32 s90, 0
	v_readlane_b32 s3, v255, 14
	v_readlane_b32 s5, v252, 25
	s_mul_i32 s2, s4, s2
	s_cselect_b32 s5, s5, s3
	s_add_i32 s5, s5, s2
	s_cmpk_lt_i32 s5, 0x800
	s_cselect_b64 s[2:3], -1, 0
	s_cmpk_gt_i32 s5, 0x7ff
	s_cbranch_scc1 .LBB0_877
	s_lshl_b32 s6, s5, 5
	s_and_b32 s6, s6, 0xf00
	s_sub_i32 s6, 0x1000, s6
	s_ashr_i32 s6, s6, 6
	v_writelane_b32 v255, s6, 43
	s_lshl_b32 s6, s5, 17
	s_and_b32 s6, s6, 0xf000000
	v_readlane_b32 s8, v255, 31
	v_readlane_b32 s9, v255, 32
	s_add_u32 s6, s8, s6
	s_addc_u32 s7, s9, 0
	s_lshl_b32 s5, s5, 7
	s_and_b32 s5, s5, 0x380
	s_add_u32 s5, s6, s5
	s_addc_u32 s6, s7, 0
	s_add_u32 s8, s5, 0x400
	s_addc_u32 s9, s6, 0
	v_writelane_b32 v255, s8, 33
	s_add_u32 s78, s5, 0x800
	s_addc_u32 s79, s6, 0
	v_writelane_b32 v255, s9, 34

.LBB0_901:
	v_and_b32_e32 v4, 64, v242
	v_xor_b32_e32 v2, 32, v242
	v_add_u32_e32 v4, 64, v4
	v_cmp_lt_i32_e32 vcc, v2, v4
	v_readlane_b32 s2, v255, 36
	v_readlane_b32 s3, v255, 37
	v_cndmask_b32_e32 v2, v242, v2, vcc
	v_lshlrev_b32_e32 v83, 2, v2
	ds_bpermute_b32 v2, v83, v214
	v_lshlrev_b32_e32 v102, 2, v206
	s_movk_i32 s84, 0xc00
	s_waitcnt lgkmcnt(0)
	v_add_f32_e32 v2, v214, v2
	v_div_scale_f32 v4, s[0:1], v2, v2, 1.0
	v_rcp_f32_e32 v5, v4
	s_nop 0
	v_fma_f32 v6, -v4, v5, 1.0
	v_fmac_f32_e32 v5, v6, v5
	v_div_scale_f32 v6, vcc, 1.0, v2, 1.0
	v_mul_f32_e32 v7, v6, v5
	v_fma_f32 v8, -v4, v7, v6
	v_fmac_f32_e32 v7, v8, v5
	v_fma_f32 v4, -v4, v7, v6
	v_div_fmas_f32 v4, v4, v5, v7
	v_div_fixup_f32 v2, v4, v2, 1.0
	ds_bpermute_b32 v4, v83, v209
	s_waitcnt lgkmcnt(0)
	v_add_f32_e32 v4, v209, v4
	v_div_scale_f32 v5, s[0:1], v4, v4, 1.0
	v_rcp_f32_e32 v6, v5
	v_readlane_b32 s0, v254, 22
	v_fma_f32 v7, -v5, v6, 1.0
	v_fmac_f32_e32 v6, v7, v6
	v_div_scale_f32 v7, vcc, 1.0, v4, 1.0
	v_mul_f32_e32 v8, v7, v6
	v_fma_f32 v9, -v5, v8, v7
	v_fmac_f32_e32 v8, v9, v6
	v_fma_f32 v5, -v5, v8, v7
	v_div_fmas_f32 v5, v5, v6, v8
	v_div_fixup_f32 v82, v5, v4, 1.0
	v_mov_b32_e32 v4, s0
	ds_read_b64 v[4:5], v4
	v_pk_mul_f32 v[42:43], v[42:43], v[82:83] op_sel_hi:[1,0]
	v_pk_mul_f32 v[38:39], v[38:39], v[82:83] op_sel_hi:[1,0]
	v_pk_mul_f32 v[42:43], v[202:203], v[42:43]
	v_pk_mul_f32 v[36:37], v[36:37], v[82:83] op_sel_hi:[1,0]
	s_waitcnt lgkmcnt(0)
	v_readfirstlane_b32 s1, v5
	v_readfirstlane_b32 s0, v4
	v_pk_mul_f32 v[4:5], v[80:81], v[82:83] op_sel_hi:[1,0]
	s_add_u32 s0, s0, s2
	v_pk_mul_f32 v[4:5], v[202:203], v[4:5]
	v_pk_fma_f32 v[42:43], v[26:27], v[2:3], v[42:43] op_sel_hi:[1,0,1] neg_lo:[0,0,1] neg_hi:[0,0,1]
	v_pk_fma_f32 v[16:17], v[64:65], v[2:3], v[4:5] op_sel_hi:[1,0,1] neg_lo:[0,0,1] neg_hi:[0,0,1]
	v_pk_mul_f32 v[4:5], v[78:79], v[82:83] op_sel_hi:[1,0]
	v_pk_mul_f32 v[26:27], v[40:41], v[82:83] op_sel_hi:[1,0]
	s_addc_u32 s1, s1, s3
	v_pk_mul_f32 v[4:5], v[202:203], v[4:5]
	v_pk_mul_f32 v[12:13], v[74:75], v[82:83] op_sel_hi:[1,0]
	v_pk_mul_f32 v[70:71], v[70:71], v[82:83] op_sel_hi:[1,0]
	v_pk_mul_f32 v[46:47], v[46:47], v[82:83] op_sel_hi:[1,0]
	v_pk_mul_f32 v[26:27], v[202:203], v[26:27]
	v_pk_mul_f32 v[38:39], v[202:203], v[38:39]
	v_pk_mul_f32 v[36:37], v[202:203], v[36:37]
	v_pk_fma_f32 v[62:63], v[62:63], v[2:3], v[4:5] op_sel_hi:[1,0,1] neg_lo:[0,0,1] neg_hi:[0,0,1]
	global_load_dwordx4 v[4:7], v102, s[0:1] offset:224
	v_pk_mul_f32 v[12:13], v[202:203], v[12:13]
	v_pk_mul_f32 v[70:71], v[202:203], v[70:71]
	v_pk_mul_f32 v[66:67], v[66:67], v[82:83] op_sel_hi:[1,0]
	v_pk_mul_f32 v[48:49], v[48:49], v[82:83] op_sel_hi:[1,0]
	v_pk_mul_f32 v[46:47], v[202:203], v[46:47]
	v_pk_fma_f32 v[40:41], v[24:25], v[2:3], v[26:27] op_sel_hi:[1,0,1] neg_lo:[0,0,1] neg_hi:[0,0,1]
	global_load_dwordx4 v[24:27], v102, s[0:1] offset:32
	v_pk_fma_f32 v[22:23], v[22:23], v[2:3], v[38:39] op_sel_hi:[1,0,1] neg_lo:[0,0,1] neg_hi:[0,0,1]
	v_pk_fma_f32 v[20:21], v[20:21], v[2:3], v[36:37] op_sel_hi:[1,0,1] neg_lo:[0,0,1] neg_hi:[0,0,1]
	global_load_dwordx4 v[36:39], v102, s[0:1]
	v_pk_mul_f32 v[8:9], v[76:77], v[82:83] op_sel_hi:[1,0]
	v_pk_fma_f32 v[58:59], v[58:59], v[2:3], v[12:13] op_sel_hi:[1,0,1] neg_lo:[0,0,1] neg_hi:[0,0,1]
	v_pk_mul_f32 v[12:13], v[72:73], v[82:83] op_sel_hi:[1,0]
	v_pk_fma_f32 v[70:71], v[54:55], v[2:3], v[70:71] op_sel_hi:[1,0,1] neg_lo:[0,0,1] neg_hi:[0,0,1]
	v_pk_mul_f32 v[54:55], v[68:69], v[82:83] op_sel_hi:[1,0]
	v_pk_mul_f32 v[66:67], v[202:203], v[66:67]
	v_pk_mul_f32 v[48:49], v[202:203], v[48:49]
	v_pk_fma_f32 v[46:47], v[30:31], v[2:3], v[46:47] op_sel_hi:[1,0,1] neg_lo:[0,0,1] neg_hi:[0,0,1]
	v_pk_mul_f32 v[30:31], v[44:45], v[82:83] op_sel_hi:[1,0]
	v_pk_mul_f32 v[8:9], v[202:203], v[8:9]
	v_pk_mul_f32 v[12:13], v[202:203], v[12:13]
	v_pk_mul_f32 v[54:55], v[202:203], v[54:55]
	v_pk_fma_f32 v[66:67], v[50:51], v[2:3], v[66:67] op_sel_hi:[1,0,1] neg_lo:[0,0,1] neg_hi:[0,0,1]
	v_pk_fma_f32 v[32:33], v[32:33], v[2:3], v[48:49] op_sel_hi:[1,0,1] neg_lo:[0,0,1] neg_hi:[0,0,1]
	global_load_dwordx4 v[48:51], v102, s[0:1] offset:96
	v_pk_mul_f32 v[30:31], v[202:203], v[30:31]
	v_pk_fma_f32 v[60:61], v[60:61], v[2:3], v[8:9] op_sel_hi:[1,0,1] neg_lo:[0,0,1] neg_hi:[0,0,1]
	global_load_dwordx4 v[8:11], v102, s[0:1] offset:192
	v_pk_fma_f32 v[56:57], v[56:57], v[2:3], v[12:13] op_sel_hi:[1,0,1] neg_lo:[0,0,1] neg_hi:[0,0,1]
	global_load_dwordx4 v[12:15], v102, s[0:1] offset:160
	v_pk_fma_f32 v[68:69], v[52:53], v[2:3], v[54:55] op_sel_hi:[1,0,1] neg_lo:[0,0,1] neg_hi:[0,0,1]
	global_load_dwordx4 v[52:55], v102, s[0:1] offset:128
	v_pk_fma_f32 v[44:45], v[28:29], v[2:3], v[30:31] op_sel_hi:[1,0,1] neg_lo:[0,0,1] neg_hi:[0,0,1]
	global_load_dwordx4 v[28:31], v102, s[0:1] offset:64
	v_pk_mul_f32 v[34:35], v[34:35], v[82:83] op_sel_hi:[1,0]
	v_pk_mul_f32 v[100:101], v[20:21], v[20:21]
	v_pk_mul_f32 v[34:35], v[202:203], v[34:35]
	v_pk_mul_f32 v[98:99], v[22:23], v[22:23]
	v_pk_fma_f32 v[18:19], v[18:19], v[2:3], v[34:35] op_sel_hi:[1,0,1] neg_lo:[0,0,1] neg_hi:[0,0,1]
	v_pk_mul_f32 v[96:97], v[40:41], v[40:41]
	v_pk_mul_f32 v[34:35], v[18:19], v[18:19]
	v_pk_mul_f32 v[94:95], v[42:43], v[42:43]
	v_add_f32_e32 v2, v34, v35
	v_add_f32_e32 v2, v100, v2
	v_add_f32_e32 v2, v101, v2
	v_add_f32_e32 v2, v98, v2
	v_add_f32_e32 v2, v99, v2
	v_add_f32_e32 v2, v96, v2
	v_add_f32_e32 v2, v97, v2
	v_add_f32_e32 v2, v94, v2
	v_pk_mul_f32 v[92:93], v[44:45], v[44:45]
	v_add_f32_e32 v2, v95, v2
	v_add_f32_e32 v2, v92, v2
	v_pk_mul_f32 v[90:91], v[46:47], v[46:47]
	v_add_f32_e32 v2, v93, v2
	v_add_f32_e32 v2, v90, v2
	v_pk_mul_f32 v[88:89], v[32:33], v[32:33]
	v_add_f32_e32 v2, v91, v2
	v_add_f32_e32 v2, v88, v2
	v_pk_mul_f32 v[86:87], v[66:67], v[66:67]
	v_add_f32_e32 v2, v89, v2
	v_add_f32_e32 v2, v86, v2
	v_pk_mul_f32 v[84:85], v[68:69], v[68:69]
	v_add_f32_e32 v2, v87, v2
	v_add_f32_e32 v2, v84, v2
	v_pk_mul_f32 v[80:81], v[70:71], v[70:71]
	v_add_f32_e32 v2, v85, v2
	v_add_f32_e32 v2, v80, v2
	v_pk_mul_f32 v[72:73], v[56:57], v[56:57]
	v_add_f32_e32 v2, v81, v2
	v_add_f32_e32 v2, v72, v2
	v_pk_mul_f32 v[74:75], v[58:59], v[58:59]
	v_add_f32_e32 v2, v73, v2
	v_add_f32_e32 v2, v74, v2
	v_pk_mul_f32 v[76:77], v[60:61], v[60:61]
	v_add_f32_e32 v2, v75, v2
	v_add_f32_e32 v2, v76, v2
	v_pk_mul_f32 v[78:79], v[62:63], v[62:63]
	v_add_f32_e32 v2, v77, v2
	v_add_f32_e32 v2, v78, v2
	v_pk_mul_f32 v[64:65], v[16:17], v[16:17]
	v_add_f32_e32 v2, v79, v2
	v_add_f32_e32 v2, v64, v2
	v_add_f32_e32 v2, v65, v2
	ds_bpermute_b32 v34, v83, v2
	v_readlane_b32 s0, v255, 29
	v_readlane_b32 s1, v255, 30
	s_movk_i32 s2, 0xc00
	s_waitcnt lgkmcnt(0)
	v_add_f32_e32 v2, v2, v34
	v_fmamk_f32 v2, v2, 0x3c800000, v237
	v_cmp_gt_f32_e32 vcc, s85, v2
	v_mul_f32_e32 v34, 0x4b800000, v2
	s_nop 0
	v_cndmask_b32_e32 v2, v2, v34, vcc
	v_rsq_f32_e32 v2, v2
	s_nop 0
	v_mul_f32_e32 v34, 0x45800000, v2
	v_cndmask_b32_e32 v2, v2, v34, vcc
	v_mul_f32_e32 v2, v212, v2
	s_waitcnt vmcnt(5)
	v_pk_mul_f32 v[34:35], v[36:37], v[2:3] op_sel_hi:[1,0]
	v_pk_mul_f32 v[6:7], v[6:7], v[2:3] op_sel_hi:[1,0]
	v_pk_mul_f32 v[18:19], v[18:19], v[34:35]
	v_pk_mul_f32 v[34:35], v[38:39], v[2:3] op_sel_hi:[1,0]
	v_pk_mul_f32 v[6:7], v[16:17], v[6:7]
	v_mov_b64_e32 v[16:17], s[0:1]
	v_pk_mul_f32 v[20:21], v[20:21], v[34:35]
	v_pk_mul_f32 v[24:25], v[24:25], v[2:3] op_sel_hi:[1,0]
	s_waitcnt vmcnt(4)
	v_pk_mul_f32 v[34:35], v[50:51], v[2:3] op_sel_hi:[1,0]
	v_mad_u64_u32 v[16:17], s[0:1], v210, s2, v[16:17]
	v_pk_mul_f32 v[22:23], v[22:23], v[24:25]
	v_pk_mul_f32 v[24:25], v[26:27], v[2:3] op_sel_hi:[1,0]
	s_waitcnt vmcnt(0)
	v_pk_mul_f32 v[26:27], v[28:29], v[2:3] op_sel_hi:[1,0]
	v_pk_mul_f32 v[28:29], v[30:31], v[2:3] op_sel_hi:[1,0]
	v_pk_mul_f32 v[30:31], v[48:49], v[2:3] op_sel_hi:[1,0]
	v_pk_mul_f32 v[32:33], v[32:33], v[34:35]
	v_pk_mul_f32 v[34:35], v[52:53], v[2:3] op_sel_hi:[1,0]
	v_pk_mul_f32 v[36:37], v[54:55], v[2:3] op_sel_hi:[1,0]
	v_pk_mul_f32 v[12:13], v[12:13], v[2:3] op_sel_hi:[1,0]
	v_pk_mul_f32 v[14:15], v[14:15], v[2:3] op_sel_hi:[1,0]
	v_pk_mul_f32 v[8:9], v[8:9], v[2:3] op_sel_hi:[1,0]
	v_pk_mul_f32 v[10:11], v[10:11], v[2:3] op_sel_hi:[1,0]
	v_pk_mul_f32 v[4:5], v[4:5], v[2:3] op_sel_hi:[1,0]
	v_mov_b32_e32 v2, v17
	v_mad_u64_u32 v[38:39], s[0:1], v211, s2, v[2:3]
	v_readlane_b32 s0, v255, 41
	v_readlane_b32 s0, v255, 45
	v_mov_b32_e32 v17, v38
	v_readlane_b32 s1, v255, 42
	s_lshl_b32 s0, s0, 1
	v_lshlrev_b32_e32 v2, 1, v206
	v_lshl_add_u64 v[16:17], v[16:17], 0, s[0:1]
	s_mov_b32 s5, s1
	v_lshl_add_u64 v[16:17], v[16:17], 0, v[2:3]
	s_mov_b64 s[0:1], 0x2f200400
	v_lshl_add_u64 v[38:39], v[16:17], 0, s[0:1]
	s_mov_b32 s0, 0x2f200000
	v_add_co_u32_e32 v16, vcc, s0, v16
	v_readlane_b32 s0, v255, 40
	s_add_i32 s2, s0, 1
	s_bitcmp0_b32 s0, 0
	v_readlane_b32 s0, v255, 15
	v_readlane_b32 s1, v255, 16
	v_pk_mul_f32 v[24:25], v[40:41], v[24:25]
	v_cvt_pk_bf16_f32 v18, v18, v19
	v_cvt_pk_bf16_f32 v19, v20, v21
	v_addc_co_u32_e32 v17, vcc, 0, v17, vcc
	v_readlane_b32 s1, v252, 25
	v_pk_mul_f32 v[26:27], v[42:43], v[26:27]
	v_pk_mul_f32 v[28:29], v[44:45], v[28:29]
	global_store_dwordx2 v[16:17], v[18:19], off offset:1024
	v_cvt_pk_bf16_f32 v16, v22, v23
	v_cvt_pk_bf16_f32 v17, v24, v25
	s_mul_i32 s0, s2, s0
	s_cselect_b32 s3, s1, s82
	v_pk_mul_f32 v[30:31], v[46:47], v[30:31]
	global_store_dwordx2 v[38:39], v[16:17], off offset:16
	v_cvt_pk_bf16_f32 v16, v26, v27
	v_cvt_pk_bf16_f32 v17, v28, v29
	s_add_i32 s3, s3, s0
	v_pk_mul_f32 v[34:35], v[66:67], v[34:35]
	v_pk_mul_f32 v[36:37], v[68:69], v[36:37]
	v_pk_mul_f32 v[12:13], v[70:71], v[12:13]
	v_pk_mul_f32 v[14:15], v[56:57], v[14:15]
	v_pk_mul_f32 v[8:9], v[58:59], v[8:9]
	v_pk_mul_f32 v[10:11], v[60:61], v[10:11]
	v_pk_mul_f32 v[4:5], v[62:63], v[4:5]
	global_store_dwordx2 v[38:39], v[16:17], off offset:32
	v_cvt_pk_bf16_f32 v16, v30, v31
	v_cvt_pk_bf16_f32 v17, v32, v33
	s_cmpk_gt_i32 s3, 0x7ff
	global_store_dwordx2 v[38:39], v[16:17], off offset:48
	v_cvt_pk_bf16_f32 v16, v34, v35
	v_cvt_pk_bf16_f32 v17, v36, v37
	v_cvt_pk_bf16_f32 v12, v12, v13
	v_cvt_pk_bf16_f32 v13, v14, v15
	v_cvt_pk_bf16_f32 v8, v8, v9
	v_cvt_pk_bf16_f32 v9, v10, v11
	v_cvt_pk_bf16_f32 v4, v4, v5
	v_cvt_pk_bf16_f32 v5, v6, v7
	s_cselect_b64 s[0:1], -1, 0
	s_cmpk_lt_i32 s3, 0x800
	global_store_dwordx2 v[38:39], v[16:17], off offset:64
	global_store_dwordx2 v[38:39], v[12:13], off offset:80
	global_store_dwordx2 v[38:39], v[8:9], off offset:96
	global_store_dwordx2 v[38:39], v[4:5], off offset:112
	s_cbranch_scc0 .LBB0_836
	s_bfe_u32 s4, s3, 0x40007
	s_and_b32 s14, s3, 7
	s_lshl_b32 s3, s3, 5
	s_and_b32 s3, s3, 0xf00
	v_writelane_b32 v255, s4, 38
	s_sub_i32 s4, 0xf00, s3
	s_sub_i32 s3, 0x1000, s3
	v_writelane_b32 v255, s4, 39
	s_ashr_i32 s75, s3, 6
	s_branch .LBB0_836

.LBB0_905:
	s_mul_i32 s0, s91, 0x4400
	s_add_i32 s2, s0, 0
	s_add_i32 s3, s2, s81
	s_add_i32 s4, s2, s33
	s_and_b64 s[0:1], s[96:97], exec
	s_cselect_b32 s0, s4, s71
	s_add_i32 s1, s2, s70
	s_mov_b32 s2, m0
	s_mov_b32 m0, s3
	s_nop 0
	global_load_lds_dwordx4 v1, s[92:93]
	s_mov_b32 m0, s0
	s_or_b64 exec, s[96:97], 1
	global_load_lds_dwordx4 v198, s[92:93]
	s_mov_b64 exec, -1
	s_mov_b32 m0, s1
	s_nop 0
	global_load_lds_dwordx4 v199, s[76:77]
	s_mov_b32 m0, s2
	s_andn2_b64 vcc, exec, s[72:73]
	s_mov_b64 s[72:73], 0
	s_cbranch_vccnz .LBB0_904
	s_add_i32 s69, s69, -1
	s_mov_b64 s[72:73], -1
	s_cmp_lg_u32 s69, 0
	s_mov_b64 s[4:5], -1
	s_cbranch_scc0 .LBB0_908
	s_add_u32 s0, s92, 0x40000
	s_addc_u32 s1, s93, 0
	s_add_u32 s2, s76, 0x40000
	s_addc_u32 s3, s77, 0
	s_mov_b64 s[4:5], 0
